# P0 compress-bias dot products: 64 serialized load pairs batched 16 at a time with counted vmcnt
# baseline (speedup 1.0000x reference)
; #define FIN(i) kin(i)
; __device__ __forceinline__ void p0_prologue(Frame& F) {
;     ...
;     for (int i = gw; i < 2 * HD; i += NGW) { const int which = i / HD, n = i % HD; const float* pe = FIN(which ? I_CVPE : I_CKPE); const float* w1 = FIN(which ? I_CVW1 : I_CKW1);
;         float s = 0.f; for (int k = F.lane; k < CMPL * HD; k += 64) s += pe[k] * w1[(size_t)k * HD + n]; s = wave_sum(s); if (F.lane == 0) ((float*)(F.ws + SM_CBIAS))[i] = s; }
.LBB0_142:
	s_add_i32 s2, s14, 0x7f
	s_cmpk_lt_u32 s2, 0xff
	s_cselect_b32 s2, s18, 0x70
	s_cselect_b32 s15, s19, 0x78
	s_add_u32 s2, s0, s2
	s_addc_u32 s3, s1, 0
	s_add_u32 s16, s0, s15
	s_addc_u32 s17, s1, 0
	s_load_dwordx2 s[24:25], s[2:3], 0x40
	s_load_dwordx2 s[34:35], s[16:17], 0x40
	s_ashr_i32 s15, s14, 31
	s_lshr_b32 s2, s15, 25
	s_add_i32 s2, s14, s2
	s_and_b32 s2, s2, 0xffffff80
	s_sub_i32 s2, s14, s2
	s_ashr_i32 s3, s2, 31
	s_waitcnt lgkmcnt(0)
	v_lshl_add_u64 v[6:7], s[34:35], 0, v[2:3]
	v_lshl_add_u64 v[4:5], s[24:25], 0, v[0:1]
	v_lshl_add_u64 v[6:7], s[2:3], 2, v[6:7]
	s_mov_b64 s[16:17], 0
	v_mov_b32_e32 v9, v8
	v_mov_b32_e32 v10, 0
	s_mov_b64 s[16:17], 0x1000
	global_load_dword v100, v[4:5], off
	global_load_dword v116, v[6:7], off
	v_lshl_add_u64 v[6:7], v[6:7], 0, s[12:13]
	global_load_dword v101, v[4:5], off offset:256
	global_load_dword v117, v[6:7], off
	v_lshl_add_u64 v[6:7], v[6:7], 0, s[12:13]
	global_load_dword v102, v[4:5], off offset:512
	global_load_dword v118, v[6:7], off
	v_lshl_add_u64 v[6:7], v[6:7], 0, s[12:13]
	global_load_dword v103, v[4:5], off offset:768
	global_load_dword v119, v[6:7], off
	v_lshl_add_u64 v[6:7], v[6:7], 0, s[12:13]
	global_load_dword v104, v[4:5], off offset:1024
	global_load_dword v120, v[6:7], off
	v_lshl_add_u64 v[6:7], v[6:7], 0, s[12:13]
	global_load_dword v105, v[4:5], off offset:1280
	global_load_dword v121, v[6:7], off
	v_lshl_add_u64 v[6:7], v[6:7], 0, s[12:13]
	global_load_dword v106, v[4:5], off offset:1536
	global_load_dword v122, v[6:7], off
	v_lshl_add_u64 v[6:7], v[6:7], 0, s[12:13]
	global_load_dword v107, v[4:5], off offset:1792
	global_load_dword v123, v[6:7], off
	v_lshl_add_u64 v[6:7], v[6:7], 0, s[12:13]
	global_load_dword v108, v[4:5], off offset:2048
	global_load_dword v124, v[6:7], off
	v_lshl_add_u64 v[6:7], v[6:7], 0, s[12:13]
	global_load_dword v109, v[4:5], off offset:2304
	global_load_dword v125, v[6:7], off
	v_lshl_add_u64 v[6:7], v[6:7], 0, s[12:13]
	global_load_dword v110, v[4:5], off offset:2560
	global_load_dword v126, v[6:7], off
	v_lshl_add_u64 v[6:7], v[6:7], 0, s[12:13]
	global_load_dword v111, v[4:5], off offset:2816
	global_load_dword v127, v[6:7], off
	v_lshl_add_u64 v[6:7], v[6:7], 0, s[12:13]
	global_load_dword v112, v[4:5], off offset:3072
	global_load_dword v128, v[6:7], off
	v_lshl_add_u64 v[6:7], v[6:7], 0, s[12:13]
	global_load_dword v113, v[4:5], off offset:3328
	global_load_dword v129, v[6:7], off
	v_lshl_add_u64 v[6:7], v[6:7], 0, s[12:13]
	global_load_dword v114, v[4:5], off offset:3584
	global_load_dword v130, v[6:7], off
	v_lshl_add_u64 v[6:7], v[6:7], 0, s[12:13]
	global_load_dword v115, v[4:5], off offset:3840
	global_load_dword v131, v[6:7], off
	v_lshl_add_u64 v[6:7], v[6:7], 0, s[12:13]
	v_lshl_add_u64 v[4:5], v[4:5], 0, s[16:17]
	s_waitcnt vmcnt(30)
	v_fmac_f32_e32 v10, v100, v116
	s_waitcnt vmcnt(28)
	v_fmac_f32_e32 v10, v101, v117
	s_waitcnt vmcnt(26)
	v_fmac_f32_e32 v10, v102, v118
	s_waitcnt vmcnt(24)
	v_fmac_f32_e32 v10, v103, v119
	s_waitcnt vmcnt(22)
	v_fmac_f32_e32 v10, v104, v120
	s_waitcnt vmcnt(20)
	v_fmac_f32_e32 v10, v105, v121
	s_waitcnt vmcnt(18)
	v_fmac_f32_e32 v10, v106, v122
	s_waitcnt vmcnt(16)
	v_fmac_f32_e32 v10, v107, v123
	s_waitcnt vmcnt(14)
	v_fmac_f32_e32 v10, v108, v124
	s_waitcnt vmcnt(12)
	v_fmac_f32_e32 v10, v109, v125
	s_waitcnt vmcnt(10)
	v_fmac_f32_e32 v10, v110, v126
	s_waitcnt vmcnt(8)
	v_fmac_f32_e32 v10, v111, v127
	s_waitcnt vmcnt(6)
	v_fmac_f32_e32 v10, v112, v128
	s_waitcnt vmcnt(4)
	v_fmac_f32_e32 v10, v113, v129
	s_waitcnt vmcnt(2)
	v_fmac_f32_e32 v10, v114, v130
	s_waitcnt vmcnt(0)
	v_fmac_f32_e32 v10, v115, v131
	global_load_dword v100, v[4:5], off
	global_load_dword v116, v[6:7], off
	v_lshl_add_u64 v[6:7], v[6:7], 0, s[12:13]
	global_load_dword v101, v[4:5], off offset:256
	global_load_dword v117, v[6:7], off
	v_lshl_add_u64 v[6:7], v[6:7], 0, s[12:13]
	global_load_dword v102, v[4:5], off offset:512
	global_load_dword v118, v[6:7], off
	v_lshl_add_u64 v[6:7], v[6:7], 0, s[12:13]
	global_load_dword v103, v[4:5], off offset:768
	global_load_dword v119, v[6:7], off
	v_lshl_add_u64 v[6:7], v[6:7], 0, s[12:13]
	global_load_dword v104, v[4:5], off offset:1024
	global_load_dword v120, v[6:7], off
	v_lshl_add_u64 v[6:7], v[6:7], 0, s[12:13]
	global_load_dword v105, v[4:5], off offset:1280
	global_load_dword v121, v[6:7], off
	v_lshl_add_u64 v[6:7], v[6:7], 0, s[12:13]
	global_load_dword v106, v[4:5], off offset:1536
	global_load_dword v122, v[6:7], off
	v_lshl_add_u64 v[6:7], v[6:7], 0, s[12:13]
	global_load_dword v107, v[4:5], off offset:1792
	global_load_dword v123, v[6:7], off
	v_lshl_add_u64 v[6:7], v[6:7], 0, s[12:13]
	global_load_dword v108, v[4:5], off offset:2048
	global_load_dword v124, v[6:7], off
	v_lshl_add_u64 v[6:7], v[6:7], 0, s[12:13]
	global_load_dword v109, v[4:5], off offset:2304
	global_load_dword v125, v[6:7], off
	v_lshl_add_u64 v[6:7], v[6:7], 0, s[12:13]
	global_load_dword v110, v[4:5], off offset:2560
	global_load_dword v126, v[6:7], off
	v_lshl_add_u64 v[6:7], v[6:7], 0, s[12:13]
	global_load_dword v111, v[4:5], off offset:2816
	global_load_dword v127, v[6:7], off
	v_lshl_add_u64 v[6:7], v[6:7], 0, s[12:13]
	global_load_dword v112, v[4:5], off offset:3072
	global_load_dword v128, v[6:7], off
	v_lshl_add_u64 v[6:7], v[6:7], 0, s[12:13]
	global_load_dword v113, v[4:5], off offset:3328
	global_load_dword v129, v[6:7], off
	v_lshl_add_u64 v[6:7], v[6:7], 0, s[12:13]
	global_load_dword v114, v[4:5], off offset:3584
	global_load_dword v130, v[6:7], off
	v_lshl_add_u64 v[6:7], v[6:7], 0, s[12:13]
	global_load_dword v115, v[4:5], off offset:3840
	global_load_dword v131, v[6:7], off
	v_lshl_add_u64 v[6:7], v[6:7], 0, s[12:13]
	v_lshl_add_u64 v[4:5], v[4:5], 0, s[16:17]
	s_waitcnt vmcnt(30)
; #define FIN(i) kin(i)
; __device__ __forceinline__ void p0_prologue(Frame& F) {
;     ...
;     for (int i = gw; i < 2 * HD; i += NGW) { const int which = i / HD, n = i % HD; const float* pe = FIN(which ? I_CVPE : I_CKPE); const float* w1 = FIN(which ? I_CVW1 : I_CKW1);
;         float s = 0.f; for (int k = F.lane; k < CMPL * HD; k += 64) s += pe[k] * w1[(size_t)k * HD + n]; s = wave_sum(s); if (F.lane == 0) ((float*)(F.ws + SM_CBIAS))[i] = s; }
	v_fmac_f32_e32 v10, v100, v116
	s_waitcnt vmcnt(28)
	v_fmac_f32_e32 v10, v101, v117
	s_waitcnt vmcnt(26)
	v_fmac_f32_e32 v10, v102, v118
	s_waitcnt vmcnt(24)
	v_fmac_f32_e32 v10, v103, v119
	s_waitcnt vmcnt(22)
	v_fmac_f32_e32 v10, v104, v120
	s_waitcnt vmcnt(20)
	v_fmac_f32_e32 v10, v105, v121
	s_waitcnt vmcnt(18)
	v_fmac_f32_e32 v10, v106, v122
	s_waitcnt vmcnt(16)
	v_fmac_f32_e32 v10, v107, v123
	s_waitcnt vmcnt(14)
	v_fmac_f32_e32 v10, v108, v124
	s_waitcnt vmcnt(12)
	v_fmac_f32_e32 v10, v109, v125
	s_waitcnt vmcnt(10)
	v_fmac_f32_e32 v10, v110, v126
	s_waitcnt vmcnt(8)
	v_fmac_f32_e32 v10, v111, v127
	s_waitcnt vmcnt(6)
	v_fmac_f32_e32 v10, v112, v128
	s_waitcnt vmcnt(4)
	v_fmac_f32_e32 v10, v113, v129
	s_waitcnt vmcnt(2)
	v_fmac_f32_e32 v10, v114, v130
	s_waitcnt vmcnt(0)
	v_fmac_f32_e32 v10, v115, v131
	global_load_dword v100, v[4:5], off
	global_load_dword v116, v[6:7], off
	v_lshl_add_u64 v[6:7], v[6:7], 0, s[12:13]
	global_load_dword v101, v[4:5], off offset:256
	global_load_dword v117, v[6:7], off
	v_lshl_add_u64 v[6:7], v[6:7], 0, s[12:13]
	global_load_dword v102, v[4:5], off offset:512
	global_load_dword v118, v[6:7], off
	v_lshl_add_u64 v[6:7], v[6:7], 0, s[12:13]
	global_load_dword v103, v[4:5], off offset:768
	global_load_dword v119, v[6:7], off
	v_lshl_add_u64 v[6:7], v[6:7], 0, s[12:13]
	global_load_dword v104, v[4:5], off offset:1024
	global_load_dword v120, v[6:7], off
	v_lshl_add_u64 v[6:7], v[6:7], 0, s[12:13]
	global_load_dword v105, v[4:5], off offset:1280
	global_load_dword v121, v[6:7], off
	v_lshl_add_u64 v[6:7], v[6:7], 0, s[12:13]
	global_load_dword v106, v[4:5], off offset:1536
	global_load_dword v122, v[6:7], off
	v_lshl_add_u64 v[6:7], v[6:7], 0, s[12:13]
	global_load_dword v107, v[4:5], off offset:1792
	global_load_dword v123, v[6:7], off
	v_lshl_add_u64 v[6:7], v[6:7], 0, s[12:13]
	global_load_dword v108, v[4:5], off offset:2048
	global_load_dword v124, v[6:7], off
	v_lshl_add_u64 v[6:7], v[6:7], 0, s[12:13]
	global_load_dword v109, v[4:5], off offset:2304
	global_load_dword v125, v[6:7], off
	v_lshl_add_u64 v[6:7], v[6:7], 0, s[12:13]
	global_load_dword v110, v[4:5], off offset:2560
	global_load_dword v126, v[6:7], off
	v_lshl_add_u64 v[6:7], v[6:7], 0, s[12:13]
	global_load_dword v111, v[4:5], off offset:2816
	global_load_dword v127, v[6:7], off
	v_lshl_add_u64 v[6:7], v[6:7], 0, s[12:13]
	global_load_dword v112, v[4:5], off offset:3072
	global_load_dword v128, v[6:7], off
	v_lshl_add_u64 v[6:7], v[6:7], 0, s[12:13]
	global_load_dword v113, v[4:5], off offset:3328
	global_load_dword v129, v[6:7], off
	v_lshl_add_u64 v[6:7], v[6:7], 0, s[12:13]
	global_load_dword v114, v[4:5], off offset:3584
	global_load_dword v130, v[6:7], off
	v_lshl_add_u64 v[6:7], v[6:7], 0, s[12:13]
	global_load_dword v115, v[4:5], off offset:3840
	global_load_dword v131, v[6:7], off
	v_lshl_add_u64 v[6:7], v[6:7], 0, s[12:13]
	v_lshl_add_u64 v[4:5], v[4:5], 0, s[16:17]
	s_waitcnt vmcnt(30)
	v_fmac_f32_e32 v10, v100, v116
	s_waitcnt vmcnt(28)
	v_fmac_f32_e32 v10, v101, v117
	s_waitcnt vmcnt(26)
	v_fmac_f32_e32 v10, v102, v118
	s_waitcnt vmcnt(24)
	v_fmac_f32_e32 v10, v103, v119
	s_waitcnt vmcnt(22)
	v_fmac_f32_e32 v10, v104, v120
	s_waitcnt vmcnt(20)
	v_fmac_f32_e32 v10, v105, v121
	s_waitcnt vmcnt(18)
	v_fmac_f32_e32 v10, v106, v122
	s_waitcnt vmcnt(16)
	v_fmac_f32_e32 v10, v107, v123
	s_waitcnt vmcnt(14)
	v_fmac_f32_e32 v10, v108, v124
	s_waitcnt vmcnt(12)
	v_fmac_f32_e32 v10, v109, v125
	s_waitcnt vmcnt(10)
	v_fmac_f32_e32 v10, v110, v126
	s_waitcnt vmcnt(8)
	v_fmac_f32_e32 v10, v111, v127
	s_waitcnt vmcnt(6)
	v_fmac_f32_e32 v10, v112, v128
	s_waitcnt vmcnt(4)
	v_fmac_f32_e32 v10, v113, v129
	s_waitcnt vmcnt(2)
	v_fmac_f32_e32 v10, v114, v130
	s_waitcnt vmcnt(0)
; #define DPP_F(v, ctrl) __builtin_bit_cast(float, __builtin_amdgcn_mov_dpp(__builtin_bit_cast(int, (v)), (ctrl), 0xF, 0xF, true))
; __device__ __forceinline__ float xsum16(float v) { float a = v, b = v; PL_SWAP16(a, b); return a + b; }
; __device__ __forceinline__ float xsum32(float v) { float a = v, b = v; PL_SWAP32(a, b); return a + b; }
; #define FIN(i) kin(i)
; __device__ __forceinline__ float wave_sum(float v) {
;     v += DPP_F(v, 0xB1); v += DPP_F(v, 0x4E); v += DPP_F(v, 0x141); v += DPP_F(v, 0x140);
;     return xsum32(xsum16(v));
; __device__ __forceinline__ void p0_prologue(Frame& F) {
;     ...
;     for (int i = gw; i < 2 * HD; i += NGW) { const int which = i / HD, n = i % HD; const float* pe = FIN(which ? I_CVPE : I_CKPE); const float* w1 = FIN(which ? I_CVW1 : I_CKW1);
;         float s = 0.f; for (int k = F.lane; k < CMPL * HD; k += 64) s += pe[k] * w1[(size_t)k * HD + n]; s = wave_sum(s); if (F.lane == 0) ((float*)(F.ws + SM_CBIAS))[i] = s; }
	v_fmac_f32_e32 v10, v115, v131
	global_load_dword v100, v[4:5], off
	global_load_dword v116, v[6:7], off
	v_lshl_add_u64 v[6:7], v[6:7], 0, s[12:13]
	global_load_dword v101, v[4:5], off offset:256
	global_load_dword v117, v[6:7], off
	v_lshl_add_u64 v[6:7], v[6:7], 0, s[12:13]
	global_load_dword v102, v[4:5], off offset:512
	global_load_dword v118, v[6:7], off
	v_lshl_add_u64 v[6:7], v[6:7], 0, s[12:13]
	global_load_dword v103, v[4:5], off offset:768
	global_load_dword v119, v[6:7], off
	v_lshl_add_u64 v[6:7], v[6:7], 0, s[12:13]
	global_load_dword v104, v[4:5], off offset:1024
	global_load_dword v120, v[6:7], off
	v_lshl_add_u64 v[6:7], v[6:7], 0, s[12:13]
	global_load_dword v105, v[4:5], off offset:1280
	global_load_dword v121, v[6:7], off
	v_lshl_add_u64 v[6:7], v[6:7], 0, s[12:13]
	global_load_dword v106, v[4:5], off offset:1536
	global_load_dword v122, v[6:7], off
	v_lshl_add_u64 v[6:7], v[6:7], 0, s[12:13]
	global_load_dword v107, v[4:5], off offset:1792
	global_load_dword v123, v[6:7], off
	v_lshl_add_u64 v[6:7], v[6:7], 0, s[12:13]
	global_load_dword v108, v[4:5], off offset:2048
	global_load_dword v124, v[6:7], off
	v_lshl_add_u64 v[6:7], v[6:7], 0, s[12:13]
	global_load_dword v109, v[4:5], off offset:2304
	global_load_dword v125, v[6:7], off
	v_lshl_add_u64 v[6:7], v[6:7], 0, s[12:13]
	global_load_dword v110, v[4:5], off offset:2560
	global_load_dword v126, v[6:7], off
	v_lshl_add_u64 v[6:7], v[6:7], 0, s[12:13]
	global_load_dword v111, v[4:5], off offset:2816
	global_load_dword v127, v[6:7], off
	v_lshl_add_u64 v[6:7], v[6:7], 0, s[12:13]
	global_load_dword v112, v[4:5], off offset:3072
	global_load_dword v128, v[6:7], off
	v_lshl_add_u64 v[6:7], v[6:7], 0, s[12:13]
	global_load_dword v113, v[4:5], off offset:3328
	global_load_dword v129, v[6:7], off
	v_lshl_add_u64 v[6:7], v[6:7], 0, s[12:13]
	global_load_dword v114, v[4:5], off offset:3584
	global_load_dword v130, v[6:7], off
	v_lshl_add_u64 v[6:7], v[6:7], 0, s[12:13]
	global_load_dword v115, v[4:5], off offset:3840
	global_load_dword v131, v[6:7], off
	v_lshl_add_u64 v[6:7], v[6:7], 0, s[12:13]
	v_lshl_add_u64 v[4:5], v[4:5], 0, s[16:17]
	s_waitcnt vmcnt(30)
	v_fmac_f32_e32 v10, v100, v116
	s_waitcnt vmcnt(28)
	v_fmac_f32_e32 v10, v101, v117
	s_waitcnt vmcnt(26)
	v_fmac_f32_e32 v10, v102, v118
	s_waitcnt vmcnt(24)
	v_fmac_f32_e32 v10, v103, v119
	s_waitcnt vmcnt(22)
	v_fmac_f32_e32 v10, v104, v120
	s_waitcnt vmcnt(20)
	v_fmac_f32_e32 v10, v105, v121
	s_waitcnt vmcnt(18)
	v_fmac_f32_e32 v10, v106, v122
	s_waitcnt vmcnt(16)
	v_fmac_f32_e32 v10, v107, v123
	s_waitcnt vmcnt(14)
	v_fmac_f32_e32 v10, v108, v124
	s_waitcnt vmcnt(12)
	v_fmac_f32_e32 v10, v109, v125
	s_waitcnt vmcnt(10)
	v_fmac_f32_e32 v10, v110, v126
	s_waitcnt vmcnt(8)
	v_fmac_f32_e32 v10, v111, v127
	s_waitcnt vmcnt(6)
	v_fmac_f32_e32 v10, v112, v128
	s_waitcnt vmcnt(4)
	v_fmac_f32_e32 v10, v113, v129
	s_waitcnt vmcnt(2)
	v_fmac_f32_e32 v10, v114, v130
	s_waitcnt vmcnt(0)
	v_fmac_f32_e32 v10, v115, v131
	s_nop 1
	v_add_f32_dpp v4, v10, v10 quad_perm:[1,0,3,2] row_mask:0xf bank_mask:0xf bound_ctrl:1
	s_nop 1
	v_add_f32_dpp v4, v4, v4 quad_perm:[2,3,0,1] row_mask:0xf bank_mask:0xf bound_ctrl:1
	s_nop 1
	v_add_f32_dpp v4, v4, v4 row_half_mirror row_mask:0xf bank_mask:0xf bound_ctrl:1
	s_nop 1
	v_add_f32_dpp v4, v4, v4 row_mirror row_mask:0xf bank_mask:0xf bound_ctrl:1
	v_mov_b32_e32 v5, v4
	s_nop 1
	v_permlane16_swap_b32 v4, v5
	s_nop 0
	v_add_f32_e32 v4, v4, v5
	v_mov_b32_e32 v5, v4
	s_nop 1
	v_permlane32_swap_b32 v4, v5
	s_and_saveexec_b64 s[2:3], vcc
	s_cbranch_execz .LBB0_141
	s_lshl_b64 s[16:17], s[14:15], 2
	s_add_u32 s16, s7, s16
	s_addc_u32 s17, s9, s17
	v_add_f32_e32 v4, v4, v5
	global_store_dword v1, v4, s[16:17]
	s_branch .LBB0_141
